# phase 0 weight transposes: the 8 broadcast gain loads per item replaced by one coalesced load + 8 ds_bpermute_b32
# speedup vs baseline: 1.0094x; 1.0065x over previous
; template <int MAPK>
; __device__ __forceinline__ void transpose_item(const float* W, int ldw, int k0, int n0, int ncnt, bf16* WT, int ldd, int dcol0, int moff, LAS float* scr, int lane, const float* gk) {
;     { const int kr = lane >> 3, c4 = (lane & 7) * 4;
;       const float* wp = W + (size_t)(k0 + kr) * ldw + n0 + c4;
;       f32x4 v[8]; float gj[8];
; #pragma unroll
;       for (int j = 0; j < 8; ++j) gj[j] = 1.0f;
;       if (gk) {
; #pragma unroll
;           for (int j = 0; j < 8; ++j) gj[j] = gk[k0 + 8 * j + kr]; }
; #pragma unroll
;       for (int j = 0; j < 8; ++j) v[j] = (c4 < ncnt) ? *(const f32x4*)(wp + (size_t)(8 * j) * ldw) : (f32x4){0.f, 0.f, 0.f, 0.f};
.LBB0_29:
	s_mul_hi_i32 s22, s29, 0x66666667
	s_lshr_b32 s23, s22, 31
	s_ashr_i32 s22, s22, 6
	s_add_i32 s23, s22, s23
	s_lshl_b32 s24, s23, 6
	v_or_b32_e32 v2, s24, v35
	v_mov_b32_e32 v90, 1.0
	v_ashrrev_i32_e32 v3, 31, v2
	v_mov_b32_e32 v64, 1.0
	s_cmp_eq_u64 s[4:5], 0
	v_mov_b32_e32 v66, 1.0
	v_mov_b32_e32 v68, 1.0
	v_mov_b32_e32 v70, 1.0
	v_mov_b32_e32 v72, 1.0
	v_mov_b32_e32 v74, 1.0
	v_mov_b32_e32 v76, 1.0
	v_mov_b32_e32 v78, 1.0
	s_cbranch_scc1 .LBB0_31
	s_lshl_b64 s[26:27], s[94:95], 2
	s_add_u32 s4, s4, s26
	s_addc_u32 s5, s5, s27
	v_lshl_add_u64 v[4:5], v[2:3], 2, s[4:5]
	v_mad_u32_u24 v92, v35, 28, v36
	v_mov_b32_e32 v93, 0
	v_lshl_add_u64 v[92:93], v[92:93], 0, v[4:5]
	global_load_dword v90, v[92:93], off

; #define LAS __attribute__((address_space(3)))
; #define LDS_WAIT() asm volatile("s_waitcnt lgkmcnt(0)" ::: "memory")
; __device__ __forceinline__ unsigned pk2(float lo, float hi) { return f2bf(lo) | (f2bf(hi) << 16); }
; template <int MAPK>
; __device__ __forceinline__ void transpose_item(const float* W, int ldw, int k0, int n0, int ncnt, bf16* WT, int ldd, int dcol0, int moff, LAS float* scr, int lane, const float* gk) {
;     ...
;       for (int j = 0; j < 8; ++j) v[j] = (c4 < ncnt) ? *(const f32x4*)(wp + (size_t)(8 * j) * ldw) : (f32x4){0.f, 0.f, 0.f, 0.f};
;       asm volatile("" : "+v"(v[0]), "+v"(v[1]), "+v"(v[2]), "+v"(v[3]), "+v"(v[4]), "+v"(v[5]), "+v"(v[6]), "+v"(v[7]) :: "memory");
; #pragma unroll
;       for (int j = 0; j < 8; ++j) v[j] = v[j] * gj[j];
; #pragma unroll
;       for (int j = 0; j < 8; ++j) { LAS float* d = scr + (8 * j + kr) * 33 + c4; d[0] = v[j].x; d[1] = v[j].y; d[2] = v[j].z; d[3] = v[j].w; } }
;     LDS_WAIT(); asm volatile("" ::: "memory");
;     const int c = lane & 7;
; #pragma unroll
;     for (int j = 0; j < 4; ++j) { const int n = (lane >> 3) + 8 * j; const LAS float* s = scr + (8 * c) * 33 + n;
;         v4u o; o.x = pk2(s[0 * 33], s[1 * 33]); o.y = pk2(s[2 * 33], s[3 * 33]); o.z = pk2(s[4 * 33], s[5 * 33]); o.w = pk2(s[6 * 33], s[7 * 33]);
;         const int sn = n0 + n - moff;
;         int drow;
;         if (MAPK == MAP_LIN) drow = sn; else if (MAPK == MAP_GATE) drow = 32 * (sn >> 4) + (sn & 15); else drow = 32 * (sn >> 4) + 16 + (sn & 15);
;         if (n < ncnt) *(v4u*)(WT + (size_t)drow * ldd + dcol0 + k0 + 8 * c) = o; }
.LBB0_47:
	s_or_b64 exec, exec, s[26:27]
	s_waitcnt vmcnt(0)
	v_lshlrev_b32_e32 v91, 2, v35
	ds_bpermute_b32 v78, v91, v90
	ds_bpermute_b32 v76, v91, v90 offset:32
	ds_bpermute_b32 v74, v91, v90 offset:64
	ds_bpermute_b32 v72, v91, v90 offset:96
	ds_bpermute_b32 v70, v91, v90 offset:128
	ds_bpermute_b32 v68, v91, v90 offset:160
	ds_bpermute_b32 v66, v91, v90 offset:192
	ds_bpermute_b32 v64, v91, v90 offset:224
	s_waitcnt lgkmcnt(0)
	v_add_u32_e32 v0, v37, v67
	v_pk_mul_f32 v[2:3], v[78:79], v[2:3] op_sel_hi:[0,1]
	v_pk_mul_f32 v[4:5], v[78:79], v[4:5] op_sel_hi:[0,1]
	v_pk_mul_f32 v[6:7], v[76:77], v[6:7] op_sel_hi:[0,1]
	ds_write2_b32 v0, v2, v3 offset1:1
	ds_write2_b32 v0, v4, v5 offset0:2 offset1:3
	v_add_u32_e32 v2, 0x420, v0
	v_pk_mul_f32 v[8:9], v[76:77], v[8:9] op_sel_hi:[0,1]
	ds_write2_b32 v2, v6, v7 offset1:1
	v_add_u32_e32 v2, 0x428, v0
	v_pk_mul_f32 v[14:15], v[74:75], v[14:15] op_sel_hi:[0,1]
	ds_write2_b32 v2, v8, v9 offset1:1
	v_add_u32_e32 v2, 0x840, v0
	v_pk_mul_f32 v[16:17], v[74:75], v[16:17] op_sel_hi:[0,1]
	ds_write2_b32 v2, v14, v15 offset1:1
	v_add_u32_e32 v2, 0x848, v0
	v_pk_mul_f32 v[10:11], v[72:73], v[10:11] op_sel_hi:[0,1]
	ds_write2_b32 v2, v16, v17 offset1:1
	v_add_u32_e32 v2, 0xc60, v0
	v_pk_mul_f32 v[12:13], v[72:73], v[12:13] op_sel_hi:[0,1]
	ds_write2_b32 v2, v10, v11 offset1:1
	v_add_u32_e32 v2, 0xc68, v0
	v_pk_mul_f32 v[22:23], v[70:71], v[22:23] op_sel_hi:[0,1]
	ds_write2_b32 v2, v12, v13 offset1:1
	v_add_u32_e32 v2, 0x1080, v0
	v_pk_mul_f32 v[24:25], v[70:71], v[24:25] op_sel_hi:[0,1]
	ds_write2_b32 v2, v22, v23 offset1:1
	v_add_u32_e32 v2, 0x1088, v0
	v_pk_mul_f32 v[18:19], v[68:69], v[18:19] op_sel_hi:[0,1]
	ds_write2_b32 v2, v24, v25 offset1:1
	v_add_u32_e32 v2, 0x14a0, v0
	v_pk_mul_f32 v[20:21], v[68:69], v[20:21] op_sel_hi:[0,1]
	ds_write2_b32 v2, v18, v19 offset1:1
	v_add_u32_e32 v2, 0x14a8, v0
	v_pk_mul_f32 v[30:31], v[66:67], v[30:31] op_sel_hi:[0,1]
	ds_write2_b32 v2, v20, v21 offset1:1
	v_add_u32_e32 v2, 0x18c0, v0
	v_pk_mul_f32 v[32:33], v[66:67], v[32:33] op_sel_hi:[0,1]
	ds_write2_b32 v2, v30, v31 offset1:1
	v_add_u32_e32 v2, 0x18c8, v0
	v_pk_mul_f32 v[28:29], v[64:65], v[28:29] op_sel_hi:[0,1]
	v_pk_mul_f32 v[26:27], v[64:65], v[26:27] op_sel_hi:[0,1]
	ds_write2_b32 v2, v32, v33 offset1:1
	v_add_u32_e32 v2, 0x1ce0, v0
	v_add_u32_e32 v0, 0x1ce8, v0
	ds_write2_b32 v2, v26, v27 offset1:1
	ds_write2_b32 v0, v28, v29 offset1:1
	s_waitcnt lgkmcnt(0)
	s_ashr_i32 s25, s24, 31
	v_lshl_add_u64 v[2:3], s[24:25], 1, v[38:39]
	v_cmp_gt_i32_e32 vcc, s30, v35
	s_and_saveexec_b64 s[4:5], vcc
	s_cbranch_execz .LBB0_51
	ds_read2_b32 v[4:5], v75 offset0:198 offset1:231
	ds_read2_b32 v[8:9], v75 offset0:132 offset1:165
	s_waitcnt lgkmcnt(1)
	v_bfe_u32 v6, v4, 16, 1
	v_bfe_u32 v0, v5, 16, 1
	v_add3_u32 v4, v4, v6, s40
	v_add3_u32 v0, v5, v0, s40
	v_lshrrev_b32_e32 v4, 16, v4
	v_and_or_b32 v7, v0, s41, v4
	ds_read2_b32 v[4:5], v75 offset0:66 offset1:99
	s_waitcnt lgkmcnt(1)
	v_bfe_u32 v6, v8, 16, 1
	v_bfe_u32 v10, v9, 16, 1
	v_add3_u32 v6, v8, v6, s40
	v_add3_u32 v0, v9, v10, s40
	v_lshrrev_b32_e32 v6, 16, v6
	ds_read2_b32 v[8:9], v75 offset1:33
	v_and_or_b32 v6, v0, s41, v6
	s_waitcnt lgkmcnt(1)
	v_bfe_u32 v0, v5, 16, 1
	v_add3_u32 v0, v5, v0, s40
	v_bfe_u32 v5, v4, 16, 1
	v_add3_u32 v4, v4, v5, s40
	v_lshrrev_b32_e32 v4, 16, v4
	v_and_or_b32 v5, v0, s41, v4
	s_waitcnt lgkmcnt(0)
	v_bfe_u32 v4, v8, 16, 1
	v_bfe_u32 v0, v9, 16, 1
	v_add3_u32 v4, v8, v4, s40
	v_add_u32_e32 v8, s22, v35
	v_add3_u32 v0, v9, v0, s40
	v_ashrrev_i32_e32 v9, 31, v8
	v_lshrrev_b32_e32 v4, 16, v4
	v_lshlrev_b64 v[8:9], 12, v[8:9]
	v_and_or_b32 v4, v0, s41, v4
	v_lshl_add_u64 v[8:9], v[2:3], 0, v[8:9]
	global_store_dwordx4 v[8:9], v[4:7], off
	s_or_b64 exec, exec, s[4:5]
	v_cmp_gt_i32_e32 vcc, s30, v69
	s_and_saveexec_b64 s[4:5], vcc
	s_cbranch_execnz .LBB0_52

; template <int MAPK>
; __device__ __forceinline__ void transpose_item(const float* W, int ldw, int k0, int n0, int ncnt, bf16* WT, int ldd, int dcol0, int moff, LAS float* scr, int lane, const float* gk) {
;     { const int kr = lane >> 3, c4 = (lane & 7) * 4;
;       const float* wp = W + (size_t)(k0 + kr) * ldw + n0 + c4;
;       f32x4 v[8]; float gj[8];
; #pragma unroll
;       for (int j = 0; j < 8; ++j) gj[j] = 1.0f;
;       if (gk) {
; #pragma unroll
;           for (int j = 0; j < 8; ++j) gj[j] = gk[k0 + 8 * j + kr]; }
; #pragma unroll
;       for (int j = 0; j < 8; ++j) v[j] = (c4 < ncnt) ? *(const f32x4*)(wp + (size_t)(8 * j) * ldw) : (f32x4){0.f, 0.f, 0.f, 0.f};
.LBB0_60:
	s_ashr_i32 s22, s30, 31
	s_lshr_b32 s22, s22, 27
	s_add_i32 s22, s30, s22
	s_ashr_i32 s23, s22, 5
	s_lshl_b32 s22, s23, 6
	v_or_b32_e32 v2, s22, v35
	v_mov_b32_e32 v90, 1.0
	v_ashrrev_i32_e32 v3, 31, v2
	v_mov_b32_e32 v64, 1.0
	s_cmp_eq_u64 s[4:5], 0
	v_mov_b32_e32 v66, 1.0
	v_mov_b32_e32 v68, 1.0
	v_mov_b32_e32 v70, 1.0
	v_mov_b32_e32 v72, 1.0
	v_mov_b32_e32 v74, 1.0
	v_mov_b32_e32 v76, 1.0
	v_mov_b32_e32 v78, 1.0
	s_cbranch_scc1 .LBB0_62
	s_lshl_b64 s[24:25], s[94:95], 2
	s_add_u32 s4, s4, s24
	s_addc_u32 s5, s5, s25
	v_lshl_add_u64 v[4:5], v[2:3], 2, s[4:5]
	v_mad_u32_u24 v92, v35, 28, v36
	v_mov_b32_e32 v93, 0
	v_lshl_add_u64 v[92:93], v[92:93], 0, v[4:5]
	global_load_dword v90, v[92:93], off

; #define LAS __attribute__((address_space(3)))
; #define LDS_WAIT() asm volatile("s_waitcnt lgkmcnt(0)" ::: "memory")
; __device__ __forceinline__ unsigned pk2(float lo, float hi) { return f2bf(lo) | (f2bf(hi) << 16); }
; template <int MAPK>
; __device__ __forceinline__ void transpose_item(const float* W, int ldw, int k0, int n0, int ncnt, bf16* WT, int ldd, int dcol0, int moff, LAS float* scr, int lane, const float* gk) {
;     ...
;       for (int j = 0; j < 8; ++j) v[j] = (c4 < ncnt) ? *(const f32x4*)(wp + (size_t)(8 * j) * ldw) : (f32x4){0.f, 0.f, 0.f, 0.f};
;       asm volatile("" : "+v"(v[0]), "+v"(v[1]), "+v"(v[2]), "+v"(v[3]), "+v"(v[4]), "+v"(v[5]), "+v"(v[6]), "+v"(v[7]) :: "memory");
; #pragma unroll
;       for (int j = 0; j < 8; ++j) v[j] = v[j] * gj[j];
; #pragma unroll
;       for (int j = 0; j < 8; ++j) { LAS float* d = scr + (8 * j + kr) * 33 + c4; d[0] = v[j].x; d[1] = v[j].y; d[2] = v[j].z; d[3] = v[j].w; } }
;     LDS_WAIT(); asm volatile("" ::: "memory");
;     const int c = lane & 7;
; #pragma unroll
;     for (int j = 0; j < 4; ++j) { const int n = (lane >> 3) + 8 * j; const LAS float* s = scr + (8 * c) * 33 + n;
;         v4u o; o.x = pk2(s[0 * 33], s[1 * 33]); o.y = pk2(s[2 * 33], s[3 * 33]); o.z = pk2(s[4 * 33], s[5 * 33]); o.w = pk2(s[6 * 33], s[7 * 33]);
;         const int sn = n0 + n - moff;
;         int drow;
;         if (MAPK == MAP_LIN) drow = sn; else if (MAPK == MAP_GATE) drow = 32 * (sn >> 4) + (sn & 15); else drow = 32 * (sn >> 4) + 16 + (sn & 15);
;         if (n < ncnt) *(v4u*)(WT + (size_t)drow * ldd + dcol0 + k0 + 8 * c) = o; }
.LBB0_78:
	s_or_b64 exec, exec, s[26:27]
	s_waitcnt vmcnt(0)
	v_lshlrev_b32_e32 v91, 2, v35
	ds_bpermute_b32 v78, v91, v90
	ds_bpermute_b32 v76, v91, v90 offset:32
	ds_bpermute_b32 v74, v91, v90 offset:64
	ds_bpermute_b32 v72, v91, v90 offset:96
	ds_bpermute_b32 v70, v91, v90 offset:128
	ds_bpermute_b32 v68, v91, v90 offset:160
	ds_bpermute_b32 v66, v91, v90 offset:192
	ds_bpermute_b32 v64, v91, v90 offset:224
	s_waitcnt lgkmcnt(0)
	v_add_u32_e32 v0, v37, v67
	v_pk_mul_f32 v[2:3], v[78:79], v[2:3] op_sel_hi:[0,1]
	v_pk_mul_f32 v[4:5], v[78:79], v[4:5] op_sel_hi:[0,1]
	v_pk_mul_f32 v[6:7], v[76:77], v[6:7] op_sel_hi:[0,1]
	ds_write2_b32 v0, v2, v3 offset1:1
	ds_write2_b32 v0, v4, v5 offset0:2 offset1:3
	v_add_u32_e32 v2, 0x420, v0
	v_pk_mul_f32 v[8:9], v[76:77], v[8:9] op_sel_hi:[0,1]
	ds_write2_b32 v2, v6, v7 offset1:1
	v_add_u32_e32 v2, 0x428, v0
	v_pk_mul_f32 v[14:15], v[74:75], v[14:15] op_sel_hi:[0,1]
	ds_write2_b32 v2, v8, v9 offset1:1
	v_add_u32_e32 v2, 0x840, v0
	v_pk_mul_f32 v[16:17], v[74:75], v[16:17] op_sel_hi:[0,1]
	ds_write2_b32 v2, v14, v15 offset1:1
	v_add_u32_e32 v2, 0x848, v0
	v_pk_mul_f32 v[10:11], v[72:73], v[10:11] op_sel_hi:[0,1]
	ds_write2_b32 v2, v16, v17 offset1:1
	v_add_u32_e32 v2, 0xc60, v0
	v_pk_mul_f32 v[12:13], v[72:73], v[12:13] op_sel_hi:[0,1]
	ds_write2_b32 v2, v10, v11 offset1:1
	v_add_u32_e32 v2, 0xc68, v0
	v_pk_mul_f32 v[22:23], v[70:71], v[22:23] op_sel_hi:[0,1]
	ds_write2_b32 v2, v12, v13 offset1:1
	v_add_u32_e32 v2, 0x1080, v0
	v_pk_mul_f32 v[24:25], v[70:71], v[24:25] op_sel_hi:[0,1]
	ds_write2_b32 v2, v22, v23 offset1:1
	v_add_u32_e32 v2, 0x1088, v0
	v_pk_mul_f32 v[18:19], v[68:69], v[18:19] op_sel_hi:[0,1]
	ds_write2_b32 v2, v24, v25 offset1:1
	v_add_u32_e32 v2, 0x14a0, v0
	v_pk_mul_f32 v[20:21], v[68:69], v[20:21] op_sel_hi:[0,1]
	ds_write2_b32 v2, v18, v19 offset1:1
	v_add_u32_e32 v2, 0x14a8, v0
	v_pk_mul_f32 v[30:31], v[66:67], v[30:31] op_sel_hi:[0,1]
	ds_write2_b32 v2, v20, v21 offset1:1
	v_add_u32_e32 v2, 0x18c0, v0
	v_pk_mul_f32 v[32:33], v[66:67], v[32:33] op_sel_hi:[0,1]
	ds_write2_b32 v2, v30, v31 offset1:1
	v_add_u32_e32 v2, 0x18c8, v0
	v_pk_mul_f32 v[28:29], v[64:65], v[28:29] op_sel_hi:[0,1]
	v_pk_mul_f32 v[26:27], v[64:65], v[26:27] op_sel_hi:[0,1]
	ds_write2_b32 v2, v32, v33 offset1:1
	v_add_u32_e32 v2, 0x1ce0, v0
	v_add_u32_e32 v0, 0x1ce8, v0
	ds_write2_b32 v2, v26, v27 offset1:1
	ds_write2_b32 v0, v28, v29 offset1:1
	s_waitcnt lgkmcnt(0)
	s_ashr_i32 s23, s22, 31
	s_addk_i32 s24, 0x1400
	v_lshl_add_u64 v[2:3], s[22:23], 1, v[38:39]
	v_cmp_gt_i32_e32 vcc, s31, v35
	s_and_saveexec_b64 s[4:5], vcc
	s_cbranch_execz .LBB0_82
	ds_read2_b32 v[4:5], v75 offset0:198 offset1:231
	ds_read2_b32 v[8:9], v75 offset0:132 offset1:165
	s_waitcnt lgkmcnt(1)
	v_bfe_u32 v6, v4, 16, 1
	v_bfe_u32 v0, v5, 16, 1
	v_add3_u32 v4, v4, v6, s40
	v_add3_u32 v0, v5, v0, s40
	v_lshrrev_b32_e32 v4, 16, v4
	v_and_or_b32 v7, v0, s41, v4
	ds_read2_b32 v[4:5], v75 offset0:66 offset1:99
	s_waitcnt lgkmcnt(1)
	v_bfe_u32 v6, v8, 16, 1
	v_bfe_u32 v10, v9, 16, 1
	v_add3_u32 v6, v8, v6, s40
	v_add3_u32 v0, v9, v10, s40
	v_lshrrev_b32_e32 v6, 16, v6
	ds_read2_b32 v[8:9], v75 offset1:33
	v_and_or_b32 v6, v0, s41, v6
	s_waitcnt lgkmcnt(1)
	v_bfe_u32 v0, v5, 16, 1
	v_add3_u32 v0, v5, v0, s40
	v_bfe_u32 v5, v4, 16, 1
	v_add3_u32 v4, v4, v5, s40
	v_lshrrev_b32_e32 v4, 16, v4
	v_and_or_b32 v5, v0, s41, v4
	s_waitcnt lgkmcnt(0)
	v_bfe_u32 v4, v8, 16, 1
	v_bfe_u32 v0, v9, 16, 1
	v_add3_u32 v4, v8, v4, s40
	v_or_b32_e32 v8, s24, v35
	v_add3_u32 v0, v9, v0, s40
	v_ashrrev_i32_e32 v9, 31, v8
	v_lshrrev_b32_e32 v4, 16, v4
	v_lshlrev_b64 v[8:9], 12, v[8:9]
	v_and_or_b32 v4, v0, s41, v4
	v_lshl_add_u64 v[8:9], v[2:3], 0, v[8:9]
	global_store_dwordx4 v[8:9], v[4:7], off
	s_or_b64 exec, exec, s[4:5]
	v_cmp_gt_i32_e32 vcc, s31, v69
	s_and_saveexec_b64 s[4:5], vcc
	s_cbranch_execnz .LBB0_83

; template <int MAPK>
; __device__ __forceinline__ void transpose_item(const float* W, int ldw, int k0, int n0, int ncnt, bf16* WT, int ldd, int dcol0, int moff, LAS float* scr, int lane, const float* gk) {
;     { const int kr = lane >> 3, c4 = (lane & 7) * 4;
;       const float* wp = W + (size_t)(k0 + kr) * ldw + n0 + c4;
;       f32x4 v[8]; float gj[8];
; #pragma unroll
;       for (int j = 0; j < 8; ++j) gj[j] = 1.0f;
;       if (gk) {
; #pragma unroll
;           for (int j = 0; j < 8; ++j) gj[j] = gk[k0 + 8 * j + kr]; }
; #pragma unroll
;       for (int j = 0; j < 8; ++j) v[j] = (c4 < ncnt) ? *(const f32x4*)(wp + (size_t)(8 * j) * ldw) : (f32x4){0.f, 0.f, 0.f, 0.f};
.LBB0_91:
	s_mul_hi_i32 s22, s31, 0x78787879
	s_lshr_b32 s23, s22, 31
	s_ashr_i32 s22, s22, 4
	s_add_i32 s23, s22, s23
	s_lshl_b32 s22, s23, 6
	v_or_b32_e32 v2, s22, v35
	v_mov_b32_e32 v90, 1.0
	v_ashrrev_i32_e32 v3, 31, v2
	v_mov_b32_e32 v64, 1.0
	s_cmp_eq_u64 s[4:5], 0
	v_mov_b32_e32 v66, 1.0
	v_mov_b32_e32 v68, 1.0
	v_mov_b32_e32 v70, 1.0
	v_mov_b32_e32 v72, 1.0
	v_mov_b32_e32 v74, 1.0
	v_mov_b32_e32 v76, 1.0
	v_mov_b32_e32 v78, 1.0
	s_cbranch_scc1 .LBB0_93
	s_lshl_b64 s[24:25], s[94:95], 2
	s_add_u32 s4, s4, s24
	s_addc_u32 s5, s5, s25
	v_lshl_add_u64 v[4:5], v[2:3], 2, s[4:5]
	v_mad_u32_u24 v92, v35, 28, v36
	v_mov_b32_e32 v93, 0
	v_lshl_add_u64 v[92:93], v[92:93], 0, v[4:5]
	global_load_dword v90, v[92:93], off

; #define LAS __attribute__((address_space(3)))
; #define LDS_WAIT() asm volatile("s_waitcnt lgkmcnt(0)" ::: "memory")
; __device__ __forceinline__ unsigned pk2(float lo, float hi) { return f2bf(lo) | (f2bf(hi) << 16); }
; template <int MAPK>
; __device__ __forceinline__ void transpose_item(const float* W, int ldw, int k0, int n0, int ncnt, bf16* WT, int ldd, int dcol0, int moff, LAS float* scr, int lane, const float* gk) {
;     ...
;       for (int j = 0; j < 8; ++j) v[j] = (c4 < ncnt) ? *(const f32x4*)(wp + (size_t)(8 * j) * ldw) : (f32x4){0.f, 0.f, 0.f, 0.f};
;       asm volatile("" : "+v"(v[0]), "+v"(v[1]), "+v"(v[2]), "+v"(v[3]), "+v"(v[4]), "+v"(v[5]), "+v"(v[6]), "+v"(v[7]) :: "memory");
; #pragma unroll
;       for (int j = 0; j < 8; ++j) v[j] = v[j] * gj[j];
; #pragma unroll
;       for (int j = 0; j < 8; ++j) { LAS float* d = scr + (8 * j + kr) * 33 + c4; d[0] = v[j].x; d[1] = v[j].y; d[2] = v[j].z; d[3] = v[j].w; } }
;     LDS_WAIT(); asm volatile("" ::: "memory");
;     const int c = lane & 7;
; #pragma unroll
;     for (int j = 0; j < 4; ++j) { const int n = (lane >> 3) + 8 * j; const LAS float* s = scr + (8 * c) * 33 + n;
;         v4u o; o.x = pk2(s[0 * 33], s[1 * 33]); o.y = pk2(s[2 * 33], s[3 * 33]); o.z = pk2(s[4 * 33], s[5 * 33]); o.w = pk2(s[6 * 33], s[7 * 33]);
;         const int sn = n0 + n - moff;
;         int drow;
;         if (MAPK == MAP_LIN) drow = sn; else if (MAPK == MAP_GATE) drow = 32 * (sn >> 4) + (sn & 15); else drow = 32 * (sn >> 4) + 16 + (sn & 15);
;         if (n < ncnt) *(v4u*)(WT + (size_t)drow * ldd + dcol0 + k0 + 8 * c) = o; }
.LBB0_109:
	s_or_b64 exec, exec, s[26:27]
	s_waitcnt vmcnt(0)
	v_lshlrev_b32_e32 v91, 2, v35
	ds_bpermute_b32 v78, v91, v90
	ds_bpermute_b32 v76, v91, v90 offset:32
	ds_bpermute_b32 v74, v91, v90 offset:64
	ds_bpermute_b32 v72, v91, v90 offset:96
	ds_bpermute_b32 v70, v91, v90 offset:128
	ds_bpermute_b32 v68, v91, v90 offset:160
	ds_bpermute_b32 v66, v91, v90 offset:192
	ds_bpermute_b32 v64, v91, v90 offset:224
	s_waitcnt lgkmcnt(0)
	v_add_u32_e32 v0, v37, v67
	v_pk_mul_f32 v[2:3], v[78:79], v[2:3] op_sel_hi:[0,1]
	v_pk_mul_f32 v[4:5], v[78:79], v[4:5] op_sel_hi:[0,1]
	v_pk_mul_f32 v[6:7], v[76:77], v[6:7] op_sel_hi:[0,1]
	ds_write2_b32 v0, v2, v3 offset1:1
	ds_write2_b32 v0, v4, v5 offset0:2 offset1:3
	v_add_u32_e32 v2, 0x420, v0
	v_pk_mul_f32 v[8:9], v[76:77], v[8:9] op_sel_hi:[0,1]
	ds_write2_b32 v2, v6, v7 offset1:1
	v_add_u32_e32 v2, 0x428, v0
	v_pk_mul_f32 v[14:15], v[74:75], v[14:15] op_sel_hi:[0,1]
	ds_write2_b32 v2, v8, v9 offset1:1
	v_add_u32_e32 v2, 0x840, v0
	v_pk_mul_f32 v[16:17], v[74:75], v[16:17] op_sel_hi:[0,1]
	ds_write2_b32 v2, v14, v15 offset1:1
	v_add_u32_e32 v2, 0x848, v0
	v_pk_mul_f32 v[10:11], v[72:73], v[10:11] op_sel_hi:[0,1]
	ds_write2_b32 v2, v16, v17 offset1:1
	v_add_u32_e32 v2, 0xc60, v0
	v_pk_mul_f32 v[12:13], v[72:73], v[12:13] op_sel_hi:[0,1]
	ds_write2_b32 v2, v10, v11 offset1:1
	v_add_u32_e32 v2, 0xc68, v0
	v_pk_mul_f32 v[22:23], v[70:71], v[22:23] op_sel_hi:[0,1]
	ds_write2_b32 v2, v12, v13 offset1:1
	v_add_u32_e32 v2, 0x1080, v0
	v_pk_mul_f32 v[24:25], v[70:71], v[24:25] op_sel_hi:[0,1]
	ds_write2_b32 v2, v22, v23 offset1:1
	v_add_u32_e32 v2, 0x1088, v0
	v_pk_mul_f32 v[18:19], v[68:69], v[18:19] op_sel_hi:[0,1]
	ds_write2_b32 v2, v24, v25 offset1:1
	v_add_u32_e32 v2, 0x14a0, v0
	v_pk_mul_f32 v[20:21], v[68:69], v[20:21] op_sel_hi:[0,1]
	ds_write2_b32 v2, v18, v19 offset1:1
	v_add_u32_e32 v2, 0x14a8, v0
	v_pk_mul_f32 v[30:31], v[66:67], v[30:31] op_sel_hi:[0,1]
	ds_write2_b32 v2, v20, v21 offset1:1
	v_add_u32_e32 v2, 0x18c0, v0
	v_pk_mul_f32 v[32:33], v[66:67], v[32:33] op_sel_hi:[0,1]
	ds_write2_b32 v2, v30, v31 offset1:1
	v_add_u32_e32 v2, 0x18c8, v0
	v_pk_mul_f32 v[28:29], v[64:65], v[28:29] op_sel_hi:[0,1]
	v_pk_mul_f32 v[26:27], v[64:65], v[26:27] op_sel_hi:[0,1]
	ds_write2_b32 v2, v32, v33 offset1:1
	v_add_u32_e32 v2, 0x1ce0, v0
	v_add_u32_e32 v0, 0x1ce8, v0
	ds_write2_b32 v2, v26, v27 offset1:1
	ds_write2_b32 v0, v28, v29 offset1:1
	s_waitcnt lgkmcnt(0)
	s_ashr_i32 s23, s22, 31
	s_addk_i32 s24, 0x1800
	v_lshl_add_u64 v[2:3], s[22:23], 1, v[38:39]
	v_cmp_gt_i32_e32 vcc, s30, v35
	s_and_saveexec_b64 s[4:5], vcc
	s_cbranch_execz .LBB0_113
	ds_read2_b32 v[4:5], v75 offset0:198 offset1:231
	ds_read2_b32 v[8:9], v75 offset0:132 offset1:165
	s_waitcnt lgkmcnt(1)
	v_bfe_u32 v6, v4, 16, 1
	v_bfe_u32 v0, v5, 16, 1
	v_add3_u32 v4, v4, v6, s40
	v_add3_u32 v0, v5, v0, s40
	v_lshrrev_b32_e32 v4, 16, v4
	v_and_or_b32 v7, v0, s41, v4
	ds_read2_b32 v[4:5], v75 offset0:66 offset1:99
	s_waitcnt lgkmcnt(1)
	v_bfe_u32 v6, v8, 16, 1
	v_bfe_u32 v10, v9, 16, 1
	v_add3_u32 v6, v8, v6, s40
	v_add3_u32 v0, v9, v10, s40
	v_lshrrev_b32_e32 v6, 16, v6
	ds_read2_b32 v[8:9], v75 offset1:33
	v_and_or_b32 v6, v0, s41, v6
	s_waitcnt lgkmcnt(1)
	v_bfe_u32 v0, v5, 16, 1
	v_add3_u32 v0, v5, v0, s40
	v_bfe_u32 v5, v4, 16, 1
	v_add3_u32 v4, v4, v5, s40
	v_lshrrev_b32_e32 v4, 16, v4
	v_and_or_b32 v5, v0, s41, v4
	s_waitcnt lgkmcnt(0)
	v_bfe_u32 v4, v8, 16, 1
	v_bfe_u32 v0, v9, 16, 1
	v_add3_u32 v4, v8, v4, s40
	v_or_b32_e32 v8, s24, v35
	v_add3_u32 v0, v9, v0, s40
	v_ashrrev_i32_e32 v9, 31, v8
	v_lshrrev_b32_e32 v4, 16, v4
	v_lshlrev_b64 v[8:9], 12, v[8:9]
	v_and_or_b32 v4, v0, s41, v4
	v_lshl_add_u64 v[8:9], v[2:3], 0, v[8:9]
	global_store_dwordx4 v[8:9], v[4:7], off
	s_or_b64 exec, exec, s[4:5]
	v_cmp_gt_i32_e32 vcc, s30, v69
	s_and_saveexec_b64 s[4:5], vcc
	s_cbranch_execnz .LBB0_114

; template <int MAPK>
; __device__ __forceinline__ void transpose_item(const float* W, int ldw, int k0, int n0, int ncnt, bf16* WT, int ldd, int dcol0, int moff, LAS float* scr, int lane, const float* gk) {
;     { const int kr = lane >> 3, c4 = (lane & 7) * 4;
;       const float* wp = W + (size_t)(k0 + kr) * ldw + n0 + c4;
;       f32x4 v[8]; float gj[8];
; #pragma unroll
;       for (int j = 0; j < 8; ++j) gj[j] = 1.0f;
;       if (gk) {
; #pragma unroll
;           for (int j = 0; j < 8; ++j) gj[j] = gk[k0 + 8 * j + kr]; }
; #pragma unroll
;       for (int j = 0; j < 8; ++j) v[j] = (c4 < ncnt) ? *(const f32x4*)(wp + (size_t)(8 * j) * ldw) : (f32x4){0.f, 0.f, 0.f, 0.f};
.LBB0_122:
	s_lshl_b32 s20, s24, 6
	v_or_b32_e32 v2, s20, v35
	v_mov_b32_e32 v90, 1.0
	v_ashrrev_i32_e32 v3, 31, v2
	v_mov_b32_e32 v64, 1.0
	s_cmp_eq_u64 s[22:23], 0
	v_mov_b32_e32 v66, 1.0
	v_mov_b32_e32 v68, 1.0
	v_mov_b32_e32 v70, 1.0
	v_mov_b32_e32 v72, 1.0
	v_mov_b32_e32 v74, 1.0
	v_mov_b32_e32 v76, 1.0
	v_mov_b32_e32 v78, 1.0
	s_cbranch_scc1 .LBB0_124
	s_lshl_b64 s[26:27], s[94:95], 2
	s_add_u32 s22, s22, s26
	s_addc_u32 s23, s23, s27
	v_lshl_add_u64 v[4:5], v[2:3], 2, s[22:23]
	v_mad_u32_u24 v92, v35, 28, v36
	v_mov_b32_e32 v93, 0
	v_lshl_add_u64 v[92:93], v[92:93], 0, v[4:5]
	global_load_dword v90, v[92:93], off

; #define LAS __attribute__((address_space(3)))
; #define LDS_WAIT() asm volatile("s_waitcnt lgkmcnt(0)" ::: "memory")
; __device__ __forceinline__ unsigned pk2(float lo, float hi) { return f2bf(lo) | (f2bf(hi) << 16); }
; template <int MAPK>
; __device__ __forceinline__ void transpose_item(const float* W, int ldw, int k0, int n0, int ncnt, bf16* WT, int ldd, int dcol0, int moff, LAS float* scr, int lane, const float* gk) {
;     ...
;       for (int j = 0; j < 8; ++j) v[j] = (c4 < ncnt) ? *(const f32x4*)(wp + (size_t)(8 * j) * ldw) : (f32x4){0.f, 0.f, 0.f, 0.f};
;       asm volatile("" : "+v"(v[0]), "+v"(v[1]), "+v"(v[2]), "+v"(v[3]), "+v"(v[4]), "+v"(v[5]), "+v"(v[6]), "+v"(v[7]) :: "memory");
; #pragma unroll
;       for (int j = 0; j < 8; ++j) v[j] = v[j] * gj[j];
; #pragma unroll
;       for (int j = 0; j < 8; ++j) { LAS float* d = scr + (8 * j + kr) * 33 + c4; d[0] = v[j].x; d[1] = v[j].y; d[2] = v[j].z; d[3] = v[j].w; } }
;     LDS_WAIT(); asm volatile("" ::: "memory");
;     const int c = lane & 7;
; #pragma unroll
;     for (int j = 0; j < 4; ++j) { const int n = (lane >> 3) + 8 * j; const LAS float* s = scr + (8 * c) * 33 + n;
;         v4u o; o.x = pk2(s[0 * 33], s[1 * 33]); o.y = pk2(s[2 * 33], s[3 * 33]); o.z = pk2(s[4 * 33], s[5 * 33]); o.w = pk2(s[6 * 33], s[7 * 33]);
;         const int sn = n0 + n - moff;
;         int drow;
;         if (MAPK == MAP_LIN) drow = sn; else if (MAPK == MAP_GATE) drow = 32 * (sn >> 4) + (sn & 15); else drow = 32 * (sn >> 4) + 16 + (sn & 15);
;         if (n < ncnt) *(v4u*)(WT + (size_t)drow * ldd + dcol0 + k0 + 8 * c) = o; }
.LBB0_140:
	s_or_b64 exec, exec, s[22:23]
	s_waitcnt vmcnt(0)
	v_lshlrev_b32_e32 v91, 2, v35
	ds_bpermute_b32 v78, v91, v90
	ds_bpermute_b32 v76, v91, v90 offset:32
	ds_bpermute_b32 v74, v91, v90 offset:64
	ds_bpermute_b32 v72, v91, v90 offset:96
	ds_bpermute_b32 v70, v91, v90 offset:128
	ds_bpermute_b32 v68, v91, v90 offset:160
	ds_bpermute_b32 v66, v91, v90 offset:192
	ds_bpermute_b32 v64, v91, v90 offset:224
	s_waitcnt lgkmcnt(0)
	v_add_u32_e32 v0, v37, v67
	v_pk_mul_f32 v[2:3], v[78:79], v[2:3] op_sel_hi:[0,1]
	v_pk_mul_f32 v[4:5], v[78:79], v[4:5] op_sel_hi:[0,1]
	v_pk_mul_f32 v[6:7], v[76:77], v[6:7] op_sel_hi:[0,1]
	ds_write2_b32 v0, v2, v3 offset1:1
	ds_write2_b32 v0, v4, v5 offset0:2 offset1:3
	v_add_u32_e32 v2, 0x420, v0
	v_pk_mul_f32 v[8:9], v[76:77], v[8:9] op_sel_hi:[0,1]
	ds_write2_b32 v2, v6, v7 offset1:1
	v_add_u32_e32 v2, 0x428, v0
	v_pk_mul_f32 v[14:15], v[74:75], v[14:15] op_sel_hi:[0,1]
	ds_write2_b32 v2, v8, v9 offset1:1
	v_add_u32_e32 v2, 0x840, v0
	v_pk_mul_f32 v[16:17], v[74:75], v[16:17] op_sel_hi:[0,1]
	ds_write2_b32 v2, v14, v15 offset1:1
	v_add_u32_e32 v2, 0x848, v0
	v_pk_mul_f32 v[10:11], v[72:73], v[10:11] op_sel_hi:[0,1]
	ds_write2_b32 v2, v16, v17 offset1:1
	v_add_u32_e32 v2, 0xc60, v0
	v_pk_mul_f32 v[12:13], v[72:73], v[12:13] op_sel_hi:[0,1]
	ds_write2_b32 v2, v10, v11 offset1:1
	v_add_u32_e32 v2, 0xc68, v0
	v_pk_mul_f32 v[22:23], v[70:71], v[22:23] op_sel_hi:[0,1]
	ds_write2_b32 v2, v12, v13 offset1:1
	v_add_u32_e32 v2, 0x1080, v0
	v_pk_mul_f32 v[24:25], v[70:71], v[24:25] op_sel_hi:[0,1]
	ds_write2_b32 v2, v22, v23 offset1:1
	v_add_u32_e32 v2, 0x1088, v0
	v_pk_mul_f32 v[18:19], v[68:69], v[18:19] op_sel_hi:[0,1]
	ds_write2_b32 v2, v24, v25 offset1:1
	v_add_u32_e32 v2, 0x14a0, v0
	v_pk_mul_f32 v[20:21], v[68:69], v[20:21] op_sel_hi:[0,1]
	ds_write2_b32 v2, v18, v19 offset1:1
	v_add_u32_e32 v2, 0x14a8, v0
	v_pk_mul_f32 v[30:31], v[66:67], v[30:31] op_sel_hi:[0,1]
	ds_write2_b32 v2, v20, v21 offset1:1
	v_add_u32_e32 v2, 0x18c0, v0
	v_pk_mul_f32 v[32:33], v[66:67], v[32:33] op_sel_hi:[0,1]
	ds_write2_b32 v2, v30, v31 offset1:1
	v_add_u32_e32 v2, 0x18c8, v0
	v_pk_mul_f32 v[28:29], v[64:65], v[28:29] op_sel_hi:[0,1]
	v_pk_mul_f32 v[26:27], v[64:65], v[26:27] op_sel_hi:[0,1]
	ds_write2_b32 v2, v32, v33 offset1:1
	v_add_u32_e32 v2, 0x1ce0, v0
	v_add_u32_e32 v0, 0x1ce8, v0
	ds_write2_b32 v2, v26, v27 offset1:1
	ds_write2_b32 v0, v28, v29 offset1:1
	s_waitcnt lgkmcnt(0)
	ds_read2_b32 v[6:7], v75 offset0:231 offset1:239
	ds_read2_b32 v[8:9], v75 offset0:198 offset1:206
	ds_read2_b32 v[12:13], v75 offset0:132 offset1:140
	ds_read2_b32 v[10:11], v75 offset0:165 offset1:173
	ds_read2_b32 v[16:17], v75 offset0:66 offset1:74
	s_waitcnt lgkmcnt(4)
	v_bfe_u32 v0, v6, 16, 1
	s_waitcnt lgkmcnt(3)
	v_bfe_u32 v2, v8, 16, 1
	v_add3_u32 v2, v8, v2, s40
	v_add3_u32 v0, v6, v0, s40
	v_lshrrev_b32_e32 v2, 16, v2
	ds_read2_b32 v[14:15], v75 offset0:99 offset1:107
	v_and_or_b32 v5, v0, s41, v2
	s_waitcnt lgkmcnt(3)
	v_bfe_u32 v2, v12, 16, 1
	s_waitcnt lgkmcnt(2)
	v_bfe_u32 v0, v10, 16, 1
	v_add3_u32 v2, v12, v2, s40
	ds_read2_b32 v[20:21], v75 offset1:8
	v_add3_u32 v0, v10, v0, s40
	v_lshrrev_b32_e32 v2, 16, v2
	ds_read2_b32 v[18:19], v75 offset0:33 offset1:41
	v_and_or_b32 v4, v0, s41, v2
	s_waitcnt lgkmcnt(3)
	v_bfe_u32 v2, v16, 16, 1
	s_waitcnt lgkmcnt(2)
	v_bfe_u32 v0, v14, 16, 1
	v_add3_u32 v2, v16, v2, s40
	v_add3_u32 v0, v14, v0, s40
	v_lshrrev_b32_e32 v2, 16, v2
	s_ashr_i32 s21, s20, 31
	v_and_or_b32 v3, v0, s41, v2
	s_waitcnt lgkmcnt(1)
	v_bfe_u32 v2, v20, 16, 1
	s_waitcnt lgkmcnt(0)
	v_bfe_u32 v0, v18, 16, 1
	v_add3_u32 v2, v20, v2, s40
	v_lshl_add_u64 v[22:23], s[20:21], 1, v[62:63]
	s_mov_b32 s20, 0x1c40000
	v_add3_u32 v0, v18, v0, s40
	v_lshrrev_b32_e32 v2, 16, v2
	v_add_co_u32_e32 v24, vcc, s20, v22
	v_and_or_b32 v2, v0, s41, v2
	s_nop 0
	v_addc_co_u32_e32 v25, vcc, 0, v23, vcc
	global_store_dwordx4 v[24:25], v[2:5], off
	v_bfe_u32 v0, v7, 16, 1
	v_add3_u32 v0, v7, v0, s40
	v_bfe_u32 v2, v9, 16, 1
	v_add3_u32 v2, v9, v2, s40
	v_lshrrev_b32_e32 v2, 16, v2
	v_and_or_b32 v5, v0, s41, v2
	v_bfe_u32 v2, v13, 16, 1
	v_bfe_u32 v0, v11, 16, 1
	v_add3_u32 v2, v13, v2, s40
	v_add3_u32 v0, v11, v0, s40
	v_lshrrev_b32_e32 v2, 16, v2
	v_and_or_b32 v4, v0, s41, v2
	v_bfe_u32 v2, v17, 16, 1
	v_bfe_u32 v0, v15, 16, 1
	v_add3_u32 v2, v17, v2, s40
	v_add3_u32 v0, v15, v0, s40
	v_lshrrev_b32_e32 v2, 16, v2
	v_and_or_b32 v3, v0, s41, v2
	v_bfe_u32 v2, v21, 16, 1
	v_bfe_u32 v0, v19, 16, 1
	v_add3_u32 v2, v21, v2, s40
	v_add3_u32 v0, v19, v0, s40
	v_lshrrev_b32_e32 v2, 16, v2
	v_add_co_u32_e32 v6, vcc, 0x1c48000, v22
	v_and_or_b32 v2, v0, s41, v2
	s_nop 0
	v_addc_co_u32_e32 v7, vcc, 0, v23, vcc
	global_store_dwordx4 v[6:7], v[2:5], off
	s_waitcnt lgkmcnt(0)
	s_mov_b32 s30, s24
	s_andn2_b64 vcc, exec, s[4:5]
	s_cbranch_vccnz .LBB0_24

; #define LAS __attribute__((address_space(3)))
; __device__ __forceinline__ void transpose_item8(const float* W, int ldw, int k0, int n0, int ncnt, unsigned char* W8, int nbase, LAS float* scr, int lane, const float* gk) {
;     ...
;       for (int j = 0; j < 8; ++j) gj[j] = gk[k0 + 8 * j + kr] * F8_SW;
; #pragma unroll
;       for (int j = 0; j < 8; ++j) v[j] = (c4 < ncnt) ? *(const f32x4*)(wp + (size_t)(8 * j) * ldw) : (f32x4){0.f, 0.f, 0.f, 0.f};
; __device__ __forceinline__ bool seg_item8(int& r, const float* W, int K, int ldw, int ns, int ncols, unsigned char* W8, LAS float* scr, int lane, const float* gk) {
;     const int nblk = (ncols + 31) / 32, cnt = (K / 64) * nblk;
;     if (r >= cnt) { r -= cnt; return false; }
;     const int kb = r / nblk, nb = r - kb * nblk, n0 = ns + 32 * nb, nc = (ncols - 32 * nb) < 32 ? (ncols - 32 * nb) : 32;
;     transpose_item8(W, ldw, 64 * kb, n0, nc, W8, ns, scr, lane, gk);
.LBB0_145:
	s_lshl_b64 s[4:5], s[94:95], 2
	s_add_u32 s4, s23, s4
	s_addc_u32 s5, s22, s5
	s_mul_hi_i32 s22, s30, 0x2aaaaaab
	s_lshr_b32 s23, s22, 31
	s_ashr_i32 s22, s22, 5
	s_add_i32 s23, s22, s23
	s_mul_i32 s22, s23, 0xffffff40
	s_add_i32 s24, s22, s30
	s_lshl_b32 s22, s24, 5
	s_sub_i32 s25, 0x1800, s22
	s_cmpk_gt_i32 s24, 0xbf
	s_cselect_b32 s31, s25, 32
	s_lshl_b32 s24, s23, 6
	v_or_b32_e32 v2, s24, v35
	v_mov_b32_e32 v90, 1.0
	v_ashrrev_i32_e32 v3, 31, v2
	v_lshl_add_u64 v[4:5], v[2:3], 2, s[4:5]
	v_mad_u32_u24 v92, v35, 28, v36
	v_mov_b32_e32 v93, 0
	v_lshl_add_u64 v[92:93], v[92:93], 0, v[4:5]
	global_load_dword v90, v[92:93], off
	v_mov_b64_e32 v[4:5], s[18:19]
	s_mov_b32 s4, 0xd140
	v_mad_i64_i32 v[2:3], s[4:5], v2, s4, v[4:5]
	s_ashr_i32 s23, s22, 31
	v_lshl_add_u64 v[2:3], s[22:23], 2, v[2:3]
	v_lshlrev_b32_e32 v0, 2, v36
	v_lshl_add_u64 v[2:3], v[2:3], 0, v[0:1]
	s_mov_b64 s[4:5], 0x7140
	v_lshl_add_u64 v[64:65], v[2:3], 0, s[4:5]
	v_cmp_gt_i32_e64 s[4:5], s31, v36
	v_mov_b32_e32 v2, 0
	v_mov_b32_e32 v6, 0
	v_mov_b32_e32 v7, 0
	v_mov_b32_e32 v8, 0
	v_mov_b32_e32 v9, 0
	s_and_saveexec_b64 s[26:27], s[4:5]
	s_cbranch_execz .LBB0_147
	global_load_dwordx4 v[6:9], v[64:65], off

; #define LAS __attribute__((address_space(3)))
; #define LDS_WAIT() asm volatile("s_waitcnt lgkmcnt(0)" ::: "memory")
; __device__ __forceinline__ unsigned pk4_fp8(float a, float b, float c, float d) { int w = __builtin_amdgcn_cvt_pk_fp8_f32(a, b, 0, false); w = __builtin_amdgcn_cvt_pk_fp8_f32(c, d, w, true); return (unsigned)w; }
; __device__ __forceinline__ void transpose_item8(const float* W, int ldw, int k0, int n0, int ncnt, unsigned char* W8, int nbase, LAS float* scr, int lane, const float* gk) {
;     ...
;       for (int j = 0; j < 8; ++j) gj[j] = gk[k0 + 8 * j + kr] * F8_SW;
; #pragma unroll
;       for (int j = 0; j < 8; ++j) v[j] = (c4 < ncnt) ? *(const f32x4*)(wp + (size_t)(8 * j) * ldw) : (f32x4){0.f, 0.f, 0.f, 0.f};
;       asm volatile("" : "+v"(v[0]), "+v"(v[1]), "+v"(v[2]), "+v"(v[3]), "+v"(v[4]), "+v"(v[5]), "+v"(v[6]), "+v"(v[7]) :: "memory");
; #pragma unroll
;       for (int j = 0; j < 8; ++j) { v[j] = v[j] * gj[j]; LAS float* d = scr + (8 * j + kr) * 33 + c4; d[0] = v[j].x; d[1] = v[j].y; d[2] = v[j].z; d[3] = v[j].w; } }
;     LDS_WAIT(); asm volatile("" ::: "memory");
;     const int c = lane & 7;
; #pragma unroll
;     for (int j = 0; j < 4; ++j) { const int n = (lane >> 3) + 8 * j; const LAS float* sp = scr + (8 * c) * 33 + n;
;         v2u o; o.x = pk4_fp8(sp[0 * 33], sp[1 * 33], sp[2 * 33], sp[3 * 33]); o.y = pk4_fp8(sp[4 * 33], sp[5 * 33], sp[6 * 33], sp[7 * 33]);
;         if (n < ncnt) *(v2u*)(W8 + (size_t)(n0 + n - nbase) * 2048 + k0 + 8 * c) = o; }
.LBB0_161:
	s_or_b64 exec, exec, s[26:27]
	s_waitcnt vmcnt(0)
	v_lshlrev_b32_e32 v91, 2, v35
	ds_bpermute_b32 v66, v91, v90
	ds_bpermute_b32 v68, v91, v90 offset:32
	ds_bpermute_b32 v70, v91, v90 offset:64
	ds_bpermute_b32 v72, v91, v90 offset:96
	ds_bpermute_b32 v74, v91, v90 offset:128
	ds_bpermute_b32 v76, v91, v90 offset:160
	ds_bpermute_b32 v78, v91, v90 offset:192
	ds_bpermute_b32 v80, v91, v90 offset:224
	s_waitcnt lgkmcnt(0)
	v_mul_f32_e32 v0, 0x43800000, v66
	v_mul_f32_e32 v64, 0x43800000, v68
	v_pk_mul_f32 v[8:9], v[0:1], v[8:9] op_sel_hi:[0,1]
	v_pk_mul_f32 v[6:7], v[0:1], v[6:7] op_sel_hi:[0,1]
	v_add_u32_e32 v0, v37, v67
	ds_write2_b32 v0, v6, v7 offset1:1
	ds_write2_b32 v0, v8, v9 offset0:2 offset1:3
	v_pk_mul_f32 v[2:3], v[64:65], v[2:3] op_sel_hi:[0,1]
	v_add_u32_e32 v6, 0x420, v0
	v_mul_f32_e32 v66, 0x43800000, v70
	v_pk_mul_f32 v[4:5], v[64:65], v[4:5] op_sel_hi:[0,1]
	ds_write2_b32 v6, v2, v3 offset1:1
	v_add_u32_e32 v2, 0x428, v0
	ds_write2_b32 v2, v4, v5 offset1:1
	v_pk_mul_f32 v[4:5], v[66:67], v[14:15] op_sel_hi:[0,1]
	v_add_u32_e32 v6, 0x840, v0
	v_mul_f32_e32 v68, 0x43800000, v72
	v_pk_mul_f32 v[2:3], v[66:67], v[16:17] op_sel_hi:[0,1]
	ds_write2_b32 v6, v4, v5 offset1:1
	v_add_u32_e32 v4, 0x848, v0
	ds_write2_b32 v4, v2, v3 offset1:1
	v_pk_mul_f32 v[4:5], v[68:69], v[10:11] op_sel_hi:[0,1]
	v_add_u32_e32 v6, 0xc60, v0
	v_mul_f32_e32 v70, 0x43800000, v74
	v_pk_mul_f32 v[2:3], v[68:69], v[12:13] op_sel_hi:[0,1]
	ds_write2_b32 v6, v4, v5 offset1:1
	v_add_u32_e32 v4, 0xc68, v0
	ds_write2_b32 v4, v2, v3 offset1:1
	v_pk_mul_f32 v[4:5], v[70:71], v[22:23] op_sel_hi:[0,1]
	v_add_u32_e32 v6, 0x1080, v0
	v_mul_f32_e32 v72, 0x43800000, v76
	v_pk_mul_f32 v[2:3], v[70:71], v[24:25] op_sel_hi:[0,1]
	ds_write2_b32 v6, v4, v5 offset1:1
	v_add_u32_e32 v4, 0x1088, v0
	ds_write2_b32 v4, v2, v3 offset1:1
	v_pk_mul_f32 v[4:5], v[72:73], v[18:19] op_sel_hi:[0,1]
	v_add_u32_e32 v6, 0x14a0, v0
	v_mul_f32_e32 v74, 0x43800000, v78
	v_pk_mul_f32 v[2:3], v[72:73], v[20:21] op_sel_hi:[0,1]
	ds_write2_b32 v6, v4, v5 offset1:1
	v_add_u32_e32 v4, 0x14a8, v0
	ds_write2_b32 v4, v2, v3 offset1:1
	v_pk_mul_f32 v[4:5], v[74:75], v[30:31] op_sel_hi:[0,1]
	v_add_u32_e32 v6, 0x18c0, v0
	v_mul_f32_e32 v76, 0x43800000, v80
	v_pk_mul_f32 v[2:3], v[74:75], v[32:33] op_sel_hi:[0,1]
	ds_write2_b32 v6, v4, v5 offset1:1
	v_add_u32_e32 v4, 0x18c8, v0
	ds_write2_b32 v4, v2, v3 offset1:1
	v_pk_mul_f32 v[2:3], v[76:77], v[28:29] op_sel_hi:[0,1]
	v_pk_mul_f32 v[4:5], v[76:77], v[26:27] op_sel_hi:[0,1]
	v_add_u32_e32 v6, 0x1ce0, v0
	v_add_u32_e32 v0, 0x1ce8, v0
	ds_write2_b32 v6, v4, v5 offset1:1
	ds_write2_b32 v0, v2, v3 offset1:1
	s_waitcnt lgkmcnt(0)
	s_ashr_i32 s25, s24, 31
	v_lshl_add_u64 v[2:3], v[40:41], 0, s[24:25]
	v_cmp_gt_i32_e32 vcc, s31, v35
	s_and_saveexec_b64 s[4:5], vcc
	s_cbranch_execz .LBB0_165
	ds_read2_b32 v[4:5], v75 offset0:132 offset1:165
	ds_read2_b32 v[6:7], v75 offset0:198 offset1:231
	ds_read2_b32 v[8:9], v75 offset1:33
	v_mov_b32_e32 v11, v1
	ds_read2_b32 v[12:13], v75 offset0:66 offset1:99
	v_mov_b32_e32 v10, v1
	s_waitcnt lgkmcnt(3)
	v_cvt_pk_fp8_f32 v11, v4, v5
	s_waitcnt lgkmcnt(1)
	v_cvt_pk_fp8_f32 v10, v8, v9
	v_or_b32_e32 v4, s22, v35
	v_ashrrev_i32_e32 v5, 31, v4
	v_cvt_pk_fp8_f32 v11, v6, v7 op_sel:[0,0,1]
	s_waitcnt lgkmcnt(0)
	v_cvt_pk_fp8_f32 v10, v12, v13 op_sel:[0,0,1]
	v_lshlrev_b64 v[4:5], 11, v[4:5]
	v_lshl_add_u64 v[4:5], v[2:3], 0, v[4:5]
	global_store_dwordx2 v[4:5], v[10:11], off
	s_or_b64 exec, exec, s[4:5]
	v_cmp_gt_i32_e32 vcc, s31, v69
	s_and_saveexec_b64 s[4:5], vcc
	s_cbranch_execnz .LBB0_166

; template <int MAPK>
; __device__ __forceinline__ void transpose_item(const float* W, int ldw, int k0, int n0, int ncnt, bf16* WT, int ldd, int dcol0, int moff, LAS float* scr, int lane, const float* gk) {
;     { const int kr = lane >> 3, c4 = (lane & 7) * 4;
;       const float* wp = W + (size_t)(k0 + kr) * ldw + n0 + c4;
;       f32x4 v[8]; float gj[8];
; #pragma unroll
;       for (int j = 0; j < 8; ++j) gj[j] = 1.0f;
;       if (gk) {
; #pragma unroll
;           for (int j = 0; j < 8; ++j) gj[j] = gk[k0 + 8 * j + kr]; }
; #pragma unroll
;       for (int j = 0; j < 8; ++j) v[j] = (c4 < ncnt) ? *(const f32x4*)(wp + (size_t)(8 * j) * ldw) : (f32x4){0.f, 0.f, 0.f, 0.f};
.LBB0_406:
	s_mul_hi_i32 s22, s26, 0x2e8ba2e9
	s_lshr_b32 s23, s22, 31
	s_ashr_i32 s22, s22, 5
	s_add_i32 s23, s22, s23
	s_lshl_b32 s22, s23, 6
	v_or_b32_e32 v2, s22, v35
	v_mov_b32_e32 v90, 1.0
	v_ashrrev_i32_e32 v3, 31, v2
	v_mov_b32_e32 v64, 1.0
	s_cmp_eq_u64 s[4:5], 0
	v_mov_b32_e32 v66, 1.0
	v_mov_b32_e32 v68, 1.0
	v_mov_b32_e32 v70, 1.0
	v_mov_b32_e32 v72, 1.0
	v_mov_b32_e32 v74, 1.0
	v_mov_b32_e32 v76, 1.0
	v_mov_b32_e32 v78, 1.0
	s_cbranch_scc1 .LBB0_408
	s_lshl_b64 s[30:31], s[94:95], 2
	s_add_u32 s4, s4, s30
	s_addc_u32 s5, s5, s31
	v_lshl_add_u64 v[4:5], v[2:3], 2, s[4:5]
	v_mad_u32_u24 v92, v35, 28, v36
	v_mov_b32_e32 v93, 0
	v_lshl_add_u64 v[92:93], v[92:93], 0, v[4:5]
	global_load_dword v90, v[92:93], off

; #define LAS __attribute__((address_space(3)))
; #define LDS_WAIT() asm volatile("s_waitcnt lgkmcnt(0)" ::: "memory")
; __device__ __forceinline__ unsigned pk2(float lo, float hi) { return f2bf(lo) | (f2bf(hi) << 16); }
; template <int MAPK>
; __device__ __forceinline__ void transpose_item(const float* W, int ldw, int k0, int n0, int ncnt, bf16* WT, int ldd, int dcol0, int moff, LAS float* scr, int lane, const float* gk) {
;     ...
;       for (int j = 0; j < 8; ++j) v[j] = (c4 < ncnt) ? *(const f32x4*)(wp + (size_t)(8 * j) * ldw) : (f32x4){0.f, 0.f, 0.f, 0.f};
;       asm volatile("" : "+v"(v[0]), "+v"(v[1]), "+v"(v[2]), "+v"(v[3]), "+v"(v[4]), "+v"(v[5]), "+v"(v[6]), "+v"(v[7]) :: "memory");
; #pragma unroll
;       for (int j = 0; j < 8; ++j) v[j] = v[j] * gj[j];
; #pragma unroll
;       for (int j = 0; j < 8; ++j) { LAS float* d = scr + (8 * j + kr) * 33 + c4; d[0] = v[j].x; d[1] = v[j].y; d[2] = v[j].z; d[3] = v[j].w; } }
;     LDS_WAIT(); asm volatile("" ::: "memory");
;     const int c = lane & 7;
; #pragma unroll
;     for (int j = 0; j < 4; ++j) { const int n = (lane >> 3) + 8 * j; const LAS float* s = scr + (8 * c) * 33 + n;
;         v4u o; o.x = pk2(s[0 * 33], s[1 * 33]); o.y = pk2(s[2 * 33], s[3 * 33]); o.z = pk2(s[4 * 33], s[5 * 33]); o.w = pk2(s[6 * 33], s[7 * 33]);
;         const int sn = n0 + n - moff;
;         int drow;
;         if (MAPK == MAP_LIN) drow = sn; else if (MAPK == MAP_GATE) drow = 32 * (sn >> 4) + (sn & 15); else drow = 32 * (sn >> 4) + 16 + (sn & 15);
;         if (n < ncnt) *(v4u*)(WT + (size_t)drow * ldd + dcol0 + k0 + 8 * c) = o; }
.LBB0_424:
	s_or_b64 exec, exec, s[24:25]
	s_waitcnt vmcnt(0)
	v_lshlrev_b32_e32 v91, 2, v35
	ds_bpermute_b32 v78, v91, v90
	ds_bpermute_b32 v76, v91, v90 offset:32
	ds_bpermute_b32 v74, v91, v90 offset:64
	ds_bpermute_b32 v72, v91, v90 offset:96
	ds_bpermute_b32 v70, v91, v90 offset:128
	ds_bpermute_b32 v68, v91, v90 offset:160
	ds_bpermute_b32 v66, v91, v90 offset:192
	ds_bpermute_b32 v64, v91, v90 offset:224
	s_waitcnt lgkmcnt(0)
	v_add_u32_e32 v0, v37, v67
	v_pk_mul_f32 v[2:3], v[78:79], v[2:3] op_sel_hi:[0,1]
	v_pk_mul_f32 v[4:5], v[78:79], v[4:5] op_sel_hi:[0,1]
	v_pk_mul_f32 v[6:7], v[76:77], v[6:7] op_sel_hi:[0,1]
	ds_write2_b32 v0, v2, v3 offset1:1
	ds_write2_b32 v0, v4, v5 offset0:2 offset1:3
	v_add_u32_e32 v2, 0x420, v0
	v_pk_mul_f32 v[8:9], v[76:77], v[8:9] op_sel_hi:[0,1]
	ds_write2_b32 v2, v6, v7 offset1:1
	v_add_u32_e32 v2, 0x428, v0
	v_pk_mul_f32 v[14:15], v[74:75], v[14:15] op_sel_hi:[0,1]
	ds_write2_b32 v2, v8, v9 offset1:1
	v_add_u32_e32 v2, 0x840, v0
	v_pk_mul_f32 v[16:17], v[74:75], v[16:17] op_sel_hi:[0,1]
	ds_write2_b32 v2, v14, v15 offset1:1
	v_add_u32_e32 v2, 0x848, v0
	v_pk_mul_f32 v[10:11], v[72:73], v[10:11] op_sel_hi:[0,1]
	ds_write2_b32 v2, v16, v17 offset1:1
	v_add_u32_e32 v2, 0xc60, v0
	v_pk_mul_f32 v[12:13], v[72:73], v[12:13] op_sel_hi:[0,1]
	ds_write2_b32 v2, v10, v11 offset1:1
	v_add_u32_e32 v2, 0xc68, v0
	v_pk_mul_f32 v[22:23], v[70:71], v[22:23] op_sel_hi:[0,1]
	ds_write2_b32 v2, v12, v13 offset1:1
	v_add_u32_e32 v2, 0x1080, v0
	v_pk_mul_f32 v[24:25], v[70:71], v[24:25] op_sel_hi:[0,1]
	ds_write2_b32 v2, v22, v23 offset1:1
	v_add_u32_e32 v2, 0x1088, v0
	v_pk_mul_f32 v[18:19], v[68:69], v[18:19] op_sel_hi:[0,1]
	ds_write2_b32 v2, v24, v25 offset1:1
	v_add_u32_e32 v2, 0x14a0, v0
	v_pk_mul_f32 v[20:21], v[68:69], v[20:21] op_sel_hi:[0,1]
	ds_write2_b32 v2, v18, v19 offset1:1
	v_add_u32_e32 v2, 0x14a8, v0
	v_pk_mul_f32 v[30:31], v[66:67], v[30:31] op_sel_hi:[0,1]
	ds_write2_b32 v2, v20, v21 offset1:1
	v_add_u32_e32 v2, 0x18c0, v0
	v_pk_mul_f32 v[32:33], v[66:67], v[32:33] op_sel_hi:[0,1]
	ds_write2_b32 v2, v30, v31 offset1:1
	v_add_u32_e32 v2, 0x18c8, v0
	v_pk_mul_f32 v[28:29], v[64:65], v[28:29] op_sel_hi:[0,1]
	v_pk_mul_f32 v[26:27], v[64:65], v[26:27] op_sel_hi:[0,1]
	ds_write2_b32 v2, v32, v33 offset1:1
	v_add_u32_e32 v2, 0x1ce0, v0
	v_add_u32_e32 v0, 0x1ce8, v0
	ds_write2_b32 v2, v26, v27 offset1:1
	ds_write2_b32 v0, v28, v29 offset1:1
	s_waitcnt lgkmcnt(0)
	s_ashr_i32 s23, s22, 31
	v_lshl_add_u64 v[2:3], s[22:23], 1, v[58:59]
	v_cmp_gt_i32_e32 vcc, s30, v35
	s_and_saveexec_b64 s[4:5], vcc
	s_cbranch_execz .LBB0_428
	ds_read2_b32 v[4:5], v75 offset0:198 offset1:231
	ds_read2_b32 v[8:9], v75 offset0:132 offset1:165
	s_movk_i32 s22, 0x1080
	s_waitcnt lgkmcnt(1)
	v_bfe_u32 v6, v4, 16, 1
	v_bfe_u32 v0, v5, 16, 1
	v_add3_u32 v4, v4, v6, s40
	v_add3_u32 v0, v5, v0, s40
	v_lshrrev_b32_e32 v4, 16, v4
	v_and_or_b32 v7, v0, s41, v4
	ds_read2_b32 v[4:5], v75 offset0:66 offset1:99
	s_waitcnt lgkmcnt(1)
	v_bfe_u32 v6, v8, 16, 1
	v_bfe_u32 v10, v9, 16, 1
	v_add3_u32 v6, v8, v6, s40
	v_add3_u32 v0, v9, v10, s40
	v_lshrrev_b32_e32 v6, 16, v6
	ds_read2_b32 v[8:9], v75 offset1:33
	v_and_or_b32 v6, v0, s41, v6
	s_waitcnt lgkmcnt(1)
	v_bfe_u32 v0, v5, 16, 1
	v_add3_u32 v0, v5, v0, s40
	v_bfe_u32 v5, v4, 16, 1
	v_add3_u32 v4, v4, v5, s40
	v_lshrrev_b32_e32 v4, 16, v4
	v_and_or_b32 v5, v0, s41, v4
	s_waitcnt lgkmcnt(0)
	v_bfe_u32 v4, v8, 16, 1
	v_bfe_u32 v0, v9, 16, 1
	v_add3_u32 v4, v8, v4, s40
	v_add3_u32 v0, v9, v0, s40
	v_lshrrev_b32_e32 v4, 16, v4
	v_and_or_b32 v4, v0, s41, v4
	v_lshl_or_b32 v0, s27, 6, v35
	v_mad_i64_i32 v[8:9], s[22:23], v0, s22, v[2:3]
	global_store_dwordx4 v[8:9], v[4:7], off
	s_or_b64 exec, exec, s[4:5]
	v_cmp_gt_i32_e32 vcc, s30, v69
	s_and_saveexec_b64 s[4:5], vcc
	s_cbranch_execnz .LBB0_429

; template <int MAPK>
; __device__ __forceinline__ void transpose_item(const float* W, int ldw, int k0, int n0, int ncnt, bf16* WT, int ldd, int dcol0, int moff, LAS float* scr, int lane, const float* gk) {
;     { const int kr = lane >> 3, c4 = (lane & 7) * 4;
;       const float* wp = W + (size_t)(k0 + kr) * ldw + n0 + c4;
;       f32x4 v[8]; float gj[8];
; #pragma unroll
;       for (int j = 0; j < 8; ++j) gj[j] = 1.0f;
;       if (gk) {
; #pragma unroll
;           for (int j = 0; j < 8; ++j) gj[j] = gk[k0 + 8 * j + kr]; }
; #pragma unroll
;       for (int j = 0; j < 8; ++j) v[j] = (c4 < ncnt) ? *(const f32x4*)(wp + (size_t)(8 * j) * ldw) : (f32x4){0.f, 0.f, 0.f, 0.f};
.LBB0_437:
	s_mul_hi_i32 s22, s27, 0x2e8ba2e9
	s_lshr_b32 s23, s22, 31
	s_ashr_i32 s22, s22, 5
	s_add_i32 s23, s22, s23
	s_lshl_b32 s22, s23, 6
	v_or_b32_e32 v2, s22, v35
	v_mov_b32_e32 v90, 1.0
	v_ashrrev_i32_e32 v3, 31, v2
	v_mov_b32_e32 v64, 1.0
	s_cmp_eq_u64 s[4:5], 0
	v_mov_b32_e32 v66, 1.0
	v_mov_b32_e32 v68, 1.0
	v_mov_b32_e32 v70, 1.0
	v_mov_b32_e32 v72, 1.0
	v_mov_b32_e32 v74, 1.0
	v_mov_b32_e32 v76, 1.0
	v_mov_b32_e32 v78, 1.0
	s_cbranch_scc1 .LBB0_439
	s_lshl_b64 s[30:31], s[94:95], 2
	s_add_u32 s4, s4, s30
	s_addc_u32 s5, s5, s31
	v_lshl_add_u64 v[4:5], v[2:3], 2, s[4:5]
	v_mad_u32_u24 v92, v35, 28, v36
	v_mov_b32_e32 v93, 0
	v_lshl_add_u64 v[92:93], v[92:93], 0, v[4:5]
	global_load_dword v90, v[92:93], off

; #define LAS __attribute__((address_space(3)))
; #define LDS_WAIT() asm volatile("s_waitcnt lgkmcnt(0)" ::: "memory")
; __device__ __forceinline__ unsigned pk2(float lo, float hi) { return f2bf(lo) | (f2bf(hi) << 16); }
; template <int MAPK>
; __device__ __forceinline__ void transpose_item(const float* W, int ldw, int k0, int n0, int ncnt, bf16* WT, int ldd, int dcol0, int moff, LAS float* scr, int lane, const float* gk) {
;     ...
;       for (int j = 0; j < 8; ++j) v[j] = (c4 < ncnt) ? *(const f32x4*)(wp + (size_t)(8 * j) * ldw) : (f32x4){0.f, 0.f, 0.f, 0.f};
;       asm volatile("" : "+v"(v[0]), "+v"(v[1]), "+v"(v[2]), "+v"(v[3]), "+v"(v[4]), "+v"(v[5]), "+v"(v[6]), "+v"(v[7]) :: "memory");
; #pragma unroll
;       for (int j = 0; j < 8; ++j) v[j] = v[j] * gj[j];
; #pragma unroll
;       for (int j = 0; j < 8; ++j) { LAS float* d = scr + (8 * j + kr) * 33 + c4; d[0] = v[j].x; d[1] = v[j].y; d[2] = v[j].z; d[3] = v[j].w; } }
;     LDS_WAIT(); asm volatile("" ::: "memory");
;     const int c = lane & 7;
; #pragma unroll
;     for (int j = 0; j < 4; ++j) { const int n = (lane >> 3) + 8 * j; const LAS float* s = scr + (8 * c) * 33 + n;
;         v4u o; o.x = pk2(s[0 * 33], s[1 * 33]); o.y = pk2(s[2 * 33], s[3 * 33]); o.z = pk2(s[4 * 33], s[5 * 33]); o.w = pk2(s[6 * 33], s[7 * 33]);
;         const int sn = n0 + n - moff;
;         int drow;
;         if (MAPK == MAP_LIN) drow = sn; else if (MAPK == MAP_GATE) drow = 32 * (sn >> 4) + (sn & 15); else drow = 32 * (sn >> 4) + 16 + (sn & 15);
;         if (n < ncnt) *(v4u*)(WT + (size_t)drow * ldd + dcol0 + k0 + 8 * c) = o; }
.LBB0_455:
	s_or_b64 exec, exec, s[24:25]
	s_waitcnt vmcnt(0)
	v_lshlrev_b32_e32 v91, 2, v35
	ds_bpermute_b32 v78, v91, v90
	ds_bpermute_b32 v76, v91, v90 offset:32
	ds_bpermute_b32 v74, v91, v90 offset:64
	ds_bpermute_b32 v72, v91, v90 offset:96
	ds_bpermute_b32 v70, v91, v90 offset:128
	ds_bpermute_b32 v68, v91, v90 offset:160
	ds_bpermute_b32 v66, v91, v90 offset:192
	ds_bpermute_b32 v64, v91, v90 offset:224
	s_waitcnt lgkmcnt(0)
	v_add_u32_e32 v0, v37, v67
	v_pk_mul_f32 v[2:3], v[78:79], v[2:3] op_sel_hi:[0,1]
	v_pk_mul_f32 v[4:5], v[78:79], v[4:5] op_sel_hi:[0,1]
	v_pk_mul_f32 v[6:7], v[76:77], v[6:7] op_sel_hi:[0,1]
	ds_write2_b32 v0, v2, v3 offset1:1
	ds_write2_b32 v0, v4, v5 offset0:2 offset1:3
	v_add_u32_e32 v2, 0x420, v0
	v_pk_mul_f32 v[8:9], v[76:77], v[8:9] op_sel_hi:[0,1]
	ds_write2_b32 v2, v6, v7 offset1:1
	v_add_u32_e32 v2, 0x428, v0
	v_pk_mul_f32 v[14:15], v[74:75], v[14:15] op_sel_hi:[0,1]
	ds_write2_b32 v2, v8, v9 offset1:1
	v_add_u32_e32 v2, 0x840, v0
	v_pk_mul_f32 v[16:17], v[74:75], v[16:17] op_sel_hi:[0,1]
	ds_write2_b32 v2, v14, v15 offset1:1
	v_add_u32_e32 v2, 0x848, v0
	v_pk_mul_f32 v[10:11], v[72:73], v[10:11] op_sel_hi:[0,1]
	ds_write2_b32 v2, v16, v17 offset1:1
	v_add_u32_e32 v2, 0xc60, v0
	v_pk_mul_f32 v[12:13], v[72:73], v[12:13] op_sel_hi:[0,1]
	ds_write2_b32 v2, v10, v11 offset1:1
	v_add_u32_e32 v2, 0xc68, v0
	v_pk_mul_f32 v[22:23], v[70:71], v[22:23] op_sel_hi:[0,1]
	ds_write2_b32 v2, v12, v13 offset1:1
	v_add_u32_e32 v2, 0x1080, v0
	v_pk_mul_f32 v[24:25], v[70:71], v[24:25] op_sel_hi:[0,1]
	ds_write2_b32 v2, v22, v23 offset1:1
	v_add_u32_e32 v2, 0x1088, v0
	v_pk_mul_f32 v[18:19], v[68:69], v[18:19] op_sel_hi:[0,1]
	ds_write2_b32 v2, v24, v25 offset1:1
	v_add_u32_e32 v2, 0x14a0, v0
	v_pk_mul_f32 v[20:21], v[68:69], v[20:21] op_sel_hi:[0,1]
	ds_write2_b32 v2, v18, v19 offset1:1
	v_add_u32_e32 v2, 0x14a8, v0
	v_pk_mul_f32 v[30:31], v[66:67], v[30:31] op_sel_hi:[0,1]
	ds_write2_b32 v2, v20, v21 offset1:1
	v_add_u32_e32 v2, 0x18c0, v0
	v_pk_mul_f32 v[32:33], v[66:67], v[32:33] op_sel_hi:[0,1]
	ds_write2_b32 v2, v30, v31 offset1:1
	v_add_u32_e32 v2, 0x18c8, v0
	v_pk_mul_f32 v[28:29], v[64:65], v[28:29] op_sel_hi:[0,1]
	v_pk_mul_f32 v[26:27], v[64:65], v[26:27] op_sel_hi:[0,1]
	ds_write2_b32 v2, v32, v33 offset1:1
	v_add_u32_e32 v2, 0x1ce0, v0
	v_add_u32_e32 v0, 0x1ce8, v0
	ds_write2_b32 v2, v26, v27 offset1:1
	ds_write2_b32 v0, v28, v29 offset1:1
	s_waitcnt lgkmcnt(0)
	s_ashr_i32 s23, s22, 31
	v_lshl_add_u64 v[2:3], s[22:23], 1, v[58:59]
	v_cmp_gt_i32_e32 vcc, s30, v35
	s_and_saveexec_b64 s[4:5], vcc
	s_cbranch_execz .LBB0_459
	ds_read2_b32 v[4:5], v75 offset0:198 offset1:231
	ds_read2_b32 v[8:9], v75 offset0:132 offset1:165
	s_movk_i32 s22, 0x1080
	s_waitcnt lgkmcnt(1)
	v_bfe_u32 v6, v4, 16, 1
	v_bfe_u32 v0, v5, 16, 1
	v_add3_u32 v4, v4, v6, s40
	v_add3_u32 v0, v5, v0, s40
	v_lshrrev_b32_e32 v4, 16, v4
	v_and_or_b32 v7, v0, s41, v4
	ds_read2_b32 v[4:5], v75 offset0:66 offset1:99
	s_waitcnt lgkmcnt(1)
	v_bfe_u32 v6, v8, 16, 1
	v_bfe_u32 v10, v9, 16, 1
	v_add3_u32 v6, v8, v6, s40
	v_add3_u32 v0, v9, v10, s40
	v_lshrrev_b32_e32 v6, 16, v6
	ds_read2_b32 v[8:9], v75 offset1:33
	v_and_or_b32 v6, v0, s41, v6
	s_waitcnt lgkmcnt(1)
	v_bfe_u32 v0, v5, 16, 1
	v_add3_u32 v0, v5, v0, s40
	v_bfe_u32 v5, v4, 16, 1
	v_add3_u32 v4, v4, v5, s40
	v_lshrrev_b32_e32 v4, 16, v4
	v_and_or_b32 v5, v0, s41, v4
	s_waitcnt lgkmcnt(0)
	v_bfe_u32 v4, v8, 16, 1
	v_bfe_u32 v0, v9, 16, 1
	v_add3_u32 v4, v8, v4, s40
	v_add3_u32 v0, v9, v0, s40
	v_lshrrev_b32_e32 v4, 16, v4
	v_and_or_b32 v4, v0, s41, v4
	v_lshl_or_b32 v0, s26, 6, v71
	v_mad_i64_i32 v[8:9], s[22:23], v0, s22, v[2:3]
	global_store_dwordx4 v[8:9], v[4:7], off
	s_or_b64 exec, exec, s[4:5]
	v_cmp_gt_i32_e32 vcc, s30, v69
	s_and_saveexec_b64 s[4:5], vcc
	s_cbranch_execnz .LBB0_460
